# baseline (speedup 1.0000x reference)
_Z7k_frontPKDF16_S0_PKfS2_S0_S2_S2_S2_PjPfS4_S4_S4_:
	s_mov_b32 s12, s3
	s_load_dwordx8 s[4:11], s[0:1], 0x0
	s_lshl_b32 s3, s2, 6
	s_ashr_i32 s13, s12, 31
	s_lshl_b64 s[14:15], s[12:13], 12
	s_ashr_i32 s16, s3, 31
	s_add_u32 s14, s14, s3
	s_addc_u32 s15, s15, s16
	s_lshl_b32 s16, s12, 22
	s_and_b32 s16, s16, 0x400000
	s_waitcnt lgkmcnt(0)
	s_add_u32 s16, s4, s16
	s_addc_u32 s17, s5, 0
	s_lshl_b32 s4, s12, 6
	s_and_b32 s4, s4, 0xffffff80
	s_ashr_i32 s5, s4, 31
	s_lshl_b64 s[4:5], s[4:5], 1
	s_add_u32 s4, s16, s4
	s_addc_u32 s5, s17, s5
	s_add_i32 s3, s3, -16
	v_lshrrev_b32_e32 v134, 4, v0
	v_lshlrev_b32_e32 v1, 4, v0
	v_mov_b32_e32 v91, 0
	v_or_b32_e32 v24, s3, v134
	v_and_b32_e32 v90, 0xf0, v1
	v_max_i32_e32 v2, 0, v24
	v_mov_b32_e32 v3, v91
	v_lshl_add_u64 v[18:19], s[4:5], 0, v[90:91]
	v_lshlrev_b64 v[2:3], 10, v[2:3]
	v_lshl_add_u64 v[10:11], v[18:19], 0, v[2:3]
	v_or_b32_e32 v2, 0x100, v0
	v_lshrrev_b32_e32 v135, 4, v2
	v_add_u32_e32 v25, s3, v135
	v_max_i32_e32 v2, 0, v25
	v_mov_b32_e32 v3, v91
	v_lshlrev_b64 v[2:3], 10, v[2:3]
	v_lshl_add_u64 v[12:13], v[18:19], 0, v[2:3]
	global_load_dwordx4 v[2:5], v[10:11], off
	global_load_dwordx4 v[6:9], v[12:13], off
	v_or_b32_e32 v10, 0x200, v0
	v_lshrrev_b32_e32 v136, 4, v10
	v_or_b32_e32 v14, 0x300, v0
	v_add_u32_e32 v30, s3, v136
	v_lshrrev_b32_e32 v137, 4, v14
	v_max_i32_e32 v10, 0, v30
	v_mov_b32_e32 v11, v91
	v_add_u32_e32 v31, s3, v137
	v_lshlrev_b64 v[10:11], 10, v[10:11]
	v_max_i32_e32 v14, 0, v31
	v_mov_b32_e32 v15, v91
	v_add_u32_e32 v32, 64, v24
	v_lshl_add_u64 v[10:11], v[18:19], 0, v[10:11]
	v_lshlrev_b64 v[14:15], 10, v[14:15]
	v_max_i32_e32 v20, 0, v32
	v_mov_b32_e32 v21, v91
	global_load_dwordx4 v[10:13], v[10:11], off
	v_lshl_add_u64 v[14:15], v[18:19], 0, v[14:15]
	v_lshlrev_b64 v[20:21], 10, v[20:21]
	global_load_dwordx4 v[14:17], v[14:15], off
	v_lshl_add_u64 v[18:19], v[18:19], 0, v[20:21]
	global_load_dwordx4 v[18:21], v[18:19], off
	v_lshrrev_b32_e32 v138, 2, v0
	v_and_b32_e32 v141, 48, v138
	v_and_b32_e32 v92, 0x3f0, v1
	v_mov_b32_e32 v23, v91
	v_lshl_or_b32 v22, v141, 10, v92
	s_movk_i32 s16, 0x2000
	v_lshl_add_u64 v[26:27], s[6:7], 0, v[22:23]
	v_add_co_u32_e32 v28, vcc, s16, v26
	global_load_dwordx4 v[74:77], v22, s[6:7]
	global_load_dwordx4 v[70:73], v22, s[6:7] offset:1024
	global_load_dwordx4 v[66:69], v22, s[6:7] offset:2048
	global_load_dwordx4 v[62:65], v22, s[6:7] offset:3072
	v_addc_co_u32_e32 v29, vcc, 0, v27, vcc
	v_cmp_lt_i32_e32 vcc, -1, v24
	global_load_dwordx4 v[50:53], v[28:29], off offset:-4096
	s_movk_i32 s3, 0x1000
	s_movk_i32 s17, 0x3000
	v_or_b32_e32 v139, 0x3c00, v1
	v_lshl_or_b32 v1, v138, 10, v139
	v_lshlrev_b32_e32 v33, 3, v0
	v_or_b32_e32 v90, 0xa500, v90
	v_and_b32_e32 v140, 15, v0
	v_and_b32_e32 v142, 48, v0
	s_movk_i32 s18, 0xc0
	v_lshlrev_b32_e32 v132, 6, v0
	v_lshlrev_b32_e32 v133, 5, v0
	s_waitcnt vmcnt(9)
	v_cndmask_b32_e32 v34, 0, v2, vcc
	v_cndmask_b32_e32 v35, 0, v3, vcc
	v_cndmask_b32_e32 v36, 0, v4, vcc
	v_cndmask_b32_e32 v37, 0, v5, vcc
	v_cmp_lt_i32_e32 vcc, -1, v25
	v_add_co_u32_e64 v2, s[4:5], s3, v26
	s_waitcnt vmcnt(8)
	v_cndmask_b32_e32 v46, 0, v6, vcc
	v_cndmask_b32_e32 v47, 0, v7, vcc
	v_cndmask_b32_e32 v48, 0, v8, vcc
	v_cndmask_b32_e32 v49, 0, v9, vcc
	v_cmp_lt_i32_e32 vcc, -1, v30
	v_addc_co_u32_e64 v3, s[4:5], 0, v27, s[4:5]
	global_load_dwordx4 v[78:81], v[2:3], off offset:1024
	global_load_dwordx4 v[82:85], v[2:3], off offset:2048
	global_load_dwordx4 v[86:89], v[2:3], off offset:3072
	s_movk_i32 s4, 0x110
	s_waitcnt vmcnt(10)
	v_cndmask_b32_e32 v94, 0, v10, vcc
	v_cndmask_b32_e32 v95, 0, v11, vcc
	v_cndmask_b32_e32 v96, 0, v12, vcc
	v_cndmask_b32_e32 v97, 0, v13, vcc
	v_cmp_lt_i32_e32 vcc, -1, v31
	v_mad_u32_u24 v106, v134, s4, v90
	v_mad_u32_u24 v130, v140, s4, v142
	s_waitcnt vmcnt(9)
	v_cndmask_b32_e32 v98, 0, v14, vcc
	v_cndmask_b32_e32 v99, 0, v15, vcc
	v_cndmask_b32_e32 v100, 0, v16, vcc
	v_cndmask_b32_e32 v101, 0, v17, vcc
	v_cmp_lt_i32_e32 vcc, -1, v32
	s_waitcnt vmcnt(8)
	s_nop 0
	v_cndmask_b32_e32 v102, 0, v18, vcc
	v_cndmask_b32_e32 v103, 0, v19, vcc
	v_cndmask_b32_e32 v104, 0, v20, vcc
	v_cndmask_b32_e32 v105, 0, v21, vcc
	v_add_co_u32_e32 v6, vcc, s17, v26
	global_load_dwordx4 v[58:61], v[28:29], off
	global_load_dwordx4 v[54:57], v[28:29], off offset:1024
	global_load_dwordx4 v[22:25], v[28:29], off offset:2048
	global_load_dwordx4 v[18:21], v[28:29], off offset:3072
	v_addc_co_u32_e32 v7, vcc, 0, v27, vcc
	global_load_dwordx4 v[14:17], v[6:7], off
	global_load_dwordx4 v[10:13], v[6:7], off offset:1024
	global_load_dwordx4 v[2:5], v[6:7], off offset:2048
	s_nop 0
	global_load_dwordx4 v[6:9], v1, s[6:7]
	v_and_b32_e32 v1, 0xf8, v33
	v_lshlrev_b32_e32 v26, 4, v1
	global_load_dwordx4 v[122:125], v26, s[8:9] offset:32
	global_load_dwordx4 v[38:41], v26, s[8:9] offset:48
	global_load_dwordx4 v[126:129], v26, s[8:9]
	global_load_dwordx4 v[42:45], v26, s[8:9] offset:16
	v_or_b32_e32 v30, 64, v26
	global_load_dwordx4 v[114:117], v30, s[8:9] offset:32
	global_load_dwordx4 v[26:29], v30, s[8:9] offset:48
	global_load_dwordx4 v[144:147], v30, s[8:9]
	s_nop 0
	global_load_dwordx4 v[30:33], v30, s[8:9] offset:16
	ds_write_b128 v106, v[34:37]
	v_mad_u32_u24 v34, v135, s4, v90
	ds_write_b128 v34, v[46:49]
	v_mad_u32_u24 v34, v136, s4, v90
	ds_write_b128 v34, v[94:97]
	v_mad_u32_u24 v34, v137, s4, v90
	v_lshlrev_b32_e32 v93, 2, v1
	ds_write_b128 v34, v[98:101]
	ds_write_b128 v106, v[102:105] offset:17408
	global_load_dwordx4 v[34:37], v93, s[10:11] offset:16
	global_load_dwordx4 v[46:49], v93, s[10:11]
	s_waitcnt lgkmcnt(0)
	s_barrier
	ds_read_b128 v[94:97], v130 offset:42240
	ds_read_b128 v[98:101], v130 offset:42304
	s_waitcnt vmcnt(25) lgkmcnt(1)
	v_mfma_f32_16x16x32_f16 a[0:3], v[74:77], v[94:97], 0
	ds_read_b128 v[102:105], v130 offset:42368
	ds_read_b128 v[106:109], v130 offset:42432
	v_and_b32_e32 v90, 12, v138
	v_and_or_b32 v90, v0, s18, v90
	s_waitcnt vmcnt(21)
	v_mfma_f32_16x16x32_f16 a[4:7], v[50:53], v[94:97], 0
	v_mul_u32_u24_e32 v93, 0x210, v140
	v_lshl_add_u32 v131, v90, 1, v93
	v_and_b32_e32 v93, 56, v138
	s_waitcnt vmcnt(17)
	v_mfma_f32_16x16x32_f16 a[8:11], v[58:61], v[94:97], 0
	v_mul_u32_u24_e32 v93, 0x210, v93
	v_lshl_add_u32 v93, v1, 1, v93
	s_load_dwordx8 s[4:11], s[0:1], 0x20
	s_waitcnt vmcnt(13)
	v_mfma_f32_16x16x32_f16 a[12:15], v[14:17], v[94:97], 0
	v_lshlrev_b32_e32 v90, 2, v0
	s_mov_b32 s18, 0xbfb8aa3b
	s_waitcnt lgkmcnt(0)
	v_mfma_f32_16x16x32_f16 a[0:3], v[70:73], v[98:101], a[0:3]
	v_mfma_f32_16x16x32_f16 a[4:7], v[78:81], v[98:101], a[4:7]
	v_mfma_f32_16x16x32_f16 a[8:11], v[54:57], v[98:101], a[8:11]
	s_waitcnt vmcnt(12)
	v_mfma_f32_16x16x32_f16 a[12:15], v[10:13], v[98:101], a[12:15]
	s_waitcnt vmcnt(9)
	v_mov_b32_e32 v98, v122
	s_waitcnt vmcnt(8)
	v_mov_b32_e32 v99, v38
	v_mov_b32_e32 v38, v123
	v_mfma_f32_16x16x32_f16 a[0:3], v[66:69], v[102:105], a[0:3]
	v_mov_b32_e32 v100, v124
	v_mov_b32_e32 v101, v40
	v_mov_b32_e32 v40, v125
	v_mfma_f32_16x16x32_f16 a[4:7], v[82:85], v[102:105], a[4:7]
	v_mfma_f32_16x16x32_f16 a[8:11], v[22:25], v[102:105], a[8:11]
	v_mfma_f32_16x16x32_f16 a[12:15], v[2:5], v[102:105], a[12:15]
	s_waitcnt vmcnt(7)
	v_mov_b32_e32 v102, v126
	s_waitcnt vmcnt(6)
	v_mov_b32_e32 v103, v42
	v_mov_b32_e32 v42, v127
	v_mfma_f32_16x16x32_f16 a[0:3], v[62:65], v[106:109], a[0:3]
	v_mov_b32_e32 v104, v128
	v_mov_b32_e32 v105, v44
	v_mov_b32_e32 v44, v129
	v_mfma_f32_16x16x32_f16 a[4:7], v[86:89], v[106:109], a[4:7]
	v_mfma_f32_16x16x32_f16 a[8:11], v[18:21], v[106:109], a[8:11]
	s_nop 2
	v_accvgpr_read_b32 v1, a0
	v_accvgpr_read_b32 v126, a1
	v_accvgpr_read_b32 v127, a2
	v_mfma_f32_16x16x32_f16 a[12:15], v[6:9], v[106:109], a[12:15]
	ds_read_b128 v[94:97], v130 offset:46592
	ds_read_b128 v[106:109], v130 offset:46656
	ds_read_b128 v[110:113], v130 offset:46720
	ds_read_b128 v[118:121], v130 offset:46784
	v_accvgpr_read_b32 v128, a3
	s_waitcnt lgkmcnt(3)
	v_mfma_f32_16x16x32_f16 a[16:19], v[74:77], v[94:97], 0
	v_cvt_pk_f16_f32 v127, v127, v128
	v_cvt_pk_f16_f32 v126, v1, v126
	v_accvgpr_read_b32 v1, a4
	v_mfma_f32_16x16x32_f16 a[20:23], v[50:53], v[94:97], 0
	v_accvgpr_read_b32 v128, a5
	v_accvgpr_read_b32 v129, a6
	v_accvgpr_read_b32 v143, a7
	v_mfma_f32_16x16x32_f16 a[24:27], v[58:61], v[94:97], 0
	v_cvt_pk_f16_f32 v129, v129, v143
	v_cvt_pk_f16_f32 v128, v1, v128
	ds_write2_b64 v131, v[126:127], v[128:129] offset1:4
	v_mfma_f32_16x16x32_f16 a[28:31], v[14:17], v[94:97], 0
	v_accvgpr_read_b32 v1, a8
	v_accvgpr_read_b32 v126, a9
	v_accvgpr_read_b32 v127, a10
	s_waitcnt lgkmcnt(3)
	v_mfma_f32_16x16x32_f16 a[16:19], v[70:73], v[106:109], a[16:19]
	v_accvgpr_read_b32 v128, a11
	ds_read_b128 v[122:125], v130 offset:51136
	v_cvt_pk_f16_f32 v127, v127, v128
	v_mfma_f32_16x16x32_f16 a[20:23], v[78:81], v[106:109], a[20:23]
	v_cvt_pk_f16_f32 v126, v1, v126
	v_accvgpr_read_b32 v1, a12
	v_accvgpr_read_b32 v128, a13
	v_mfma_f32_16x16x32_f16 a[24:27], v[54:57], v[106:109], a[24:27]
	v_accvgpr_read_b32 v129, a14
	v_accvgpr_read_b32 v143, a15
	v_cvt_pk_f16_f32 v129, v129, v143
	v_mfma_f32_16x16x32_f16 a[28:31], v[10:13], v[106:109], a[28:31]
	ds_read_b128 v[106:109], v130 offset:50944
	v_cvt_pk_f16_f32 v128, v1, v128
	ds_write2_b64 v131, v[126:127], v[128:129] offset0:8 offset1:12
	s_waitcnt lgkmcnt(5)
	v_mfma_f32_16x16x32_f16 a[16:19], v[66:69], v[110:113], a[16:19]
	s_waitcnt vmcnt(3)
	v_mov_b32_e32 v94, v144
	s_waitcnt vmcnt(2)
	v_mov_b32_e32 v95, v30
	v_mov_b32_e32 v30, v145
	v_mfma_f32_16x16x32_f16 a[20:23], v[82:85], v[110:113], a[20:23]
	v_mov_b32_e32 v96, v146
	v_mov_b32_e32 v97, v32
	v_mov_b32_e32 v32, v147
	v_mfma_f32_16x16x32_f16 a[24:27], v[22:25], v[110:113], a[24:27]
	v_mfma_f32_16x16x32_f16 a[28:31], v[2:5], v[110:113], a[28:31]
	ds_read_b128 v[110:113], v130 offset:51008
	s_waitcnt lgkmcnt(2)
	v_mfma_f32_16x16x32_f16 a[32:35], v[74:77], v[106:109], 0
	v_mfma_f32_16x16x32_f16 a[0:3], v[50:53], v[106:109], 0
	v_mfma_f32_16x16x32_f16 a[16:19], v[62:65], v[118:121], a[16:19]
	v_mfma_f32_16x16x32_f16 a[20:23], v[86:89], v[118:121], a[20:23]
	v_mfma_f32_16x16x32_f16 a[24:27], v[18:21], v[118:121], a[24:27]
	s_nop 5
	v_accvgpr_read_b32 v1, a16
	v_accvgpr_read_b32 v126, a17
	v_accvgpr_read_b32 v127, a18
	v_mfma_f32_16x16x32_f16 a[28:31], v[6:9], v[118:121], a[28:31]
	ds_read_b128 v[118:121], v130 offset:51072
	v_accvgpr_read_b32 v128, a19
	v_cvt_pk_f16_f32 v126, v1, v126
	v_mfma_f32_16x16x32_f16 a[4:7], v[58:61], v[106:109], 0
	v_accvgpr_read_b32 v1, a20
	v_cvt_pk_f16_f32 v127, v127, v128
	v_accvgpr_read_b32 v128, a25
	s_waitcnt lgkmcnt(1)
	v_mfma_f32_16x16x32_f16 a[32:35], v[70:73], v[110:113], a[32:35]
	v_accvgpr_read_b32 v129, a27
	v_accvgpr_read_b32 v143, a29
	v_accvgpr_read_b32 v144, a31
	v_mfma_f32_16x16x32_f16 a[8:11], v[14:17], v[106:109], 0
	v_accvgpr_read_b32 v106, a21
	v_accvgpr_read_b32 v107, a22
	v_accvgpr_read_b32 v108, a23
	v_mfma_f32_16x16x32_f16 a[0:3], v[78:81], v[110:113], a[0:3]
	v_mfma_f32_16x16x32_f16 a[4:7], v[54:57], v[110:113], a[4:7]
	s_waitcnt lgkmcnt(0)
	v_mfma_f32_16x16x32_f16 a[32:35], v[66:69], v[118:121], a[32:35]
	v_mfma_f32_16x16x32_f16 a[8:11], v[10:13], v[110:113], a[8:11]
	v_cvt_pk_f16_f32 v111, v107, v108
	v_cvt_pk_f16_f32 v110, v1, v106
	v_add_u32_e32 v1, 0x2000, v131
	v_mfma_f32_16x16x32_f16 a[0:3], v[82:85], v[118:121], a[0:3]
	ds_write2_b64 v1, v[126:127], v[110:111] offset0:32 offset1:36
	v_accvgpr_read_b32 v126, a24
	v_accvgpr_read_b32 v127, a26
	v_mfma_f32_16x16x32_f16 a[4:7], v[22:25], v[118:121], a[4:7]
	ds_read_b128 v[106:109], v130 offset:55296
	ds_read_b128 v[110:113], v130 offset:55360
	v_cvt_pk_f16_f32 v127, v127, v129
	v_mfma_f32_16x16x32_f16 a[32:35], v[62:65], v[122:125], a[32:35]
	v_cvt_pk_f16_f32 v126, v126, v128
	v_accvgpr_read_b32 v128, a28
	v_accvgpr_read_b32 v129, a30
	v_mfma_f32_16x16x32_f16 a[8:11], v[2:5], v[118:121], a[8:11]
	v_cvt_pk_f16_f32 v129, v129, v144
	v_cvt_pk_f16_f32 v128, v128, v143
	ds_write2_b64 v1, v[126:127], v[128:129] offset0:40 offset1:44
	v_mfma_f32_16x16x32_f16 a[0:3], v[86:89], v[122:125], a[0:3]
	v_accvgpr_read_b32 v1, a32
	v_accvgpr_read_b32 v126, a33
	v_accvgpr_read_b32 v127, a34
	v_mfma_f32_16x16x32_f16 a[4:7], v[18:21], v[122:125], a[4:7]
	v_accvgpr_read_b32 v128, a35
	v_cvt_pk_f16_f32 v127, v127, v128
	v_cvt_pk_f16_f32 v126, v1, v126
	v_mfma_f32_16x16x32_f16 a[8:11], v[6:9], v[122:125], a[8:11]
	v_accvgpr_read_b32 v1, a0
	v_accvgpr_read_b32 v128, a1
	v_accvgpr_read_b32 v129, a2
	v_accvgpr_read_b32 v143, a3
	v_cvt_pk_f16_f32 v129, v129, v143
	v_cvt_pk_f16_f32 v128, v1, v128
	v_add_u32_e32 v1, 0x4000, v131
	s_waitcnt lgkmcnt(2)
	v_mfma_f32_16x16x32_f16 a[12:15], v[74:77], v[106:109], 0
	ds_write2_b64 v1, v[126:127], v[128:129] offset0:64 offset1:68
	v_accvgpr_read_b32 v126, a4
	v_accvgpr_read_b32 v128, a5
	v_mfma_f32_16x16x32_f16 a[16:19], v[50:53], v[106:109], 0
	v_accvgpr_read_b32 v127, a6
	v_accvgpr_read_b32 v129, a7
	v_cvt_pk_f16_f32 v126, v126, v128
	v_mfma_f32_16x16x32_f16 a[20:23], v[58:61], v[106:109], 0
	v_accvgpr_read_b32 v128, a8
	v_cvt_pk_f16_f32 v127, v127, v129
	ds_read_b128 v[118:121], v130 offset:55424
	ds_read_b128 v[122:125], v130 offset:55488
	v_mfma_f32_16x16x32_f16 a[4:7], v[14:17], v[106:109], 0
	v_accvgpr_read_b32 v106, a9
	v_accvgpr_read_b32 v107, a10
	v_accvgpr_read_b32 v108, a11
	v_cvt_pk_f16_f32 v107, v107, v108
	v_cvt_pk_f16_f32 v106, v128, v106
	ds_write2_b64 v1, v[126:127], v[106:107] offset0:72 offset1:76
	ds_read_b128 v[106:109], v130 offset:59648
	s_waitcnt lgkmcnt(6)
	v_mfma_f32_16x16x32_f16 a[12:15], v[70:73], v[110:113], a[12:15]
	v_mfma_f32_16x16x32_f16 a[16:19], v[78:81], v[110:113], a[16:19]
	v_mfma_f32_16x16x32_f16 a[0:3], v[54:57], v[110:113], a[20:23]
	v_mfma_f32_16x16x32_f16 a[4:7], v[10:13], v[110:113], a[4:7]
	ds_read_b128 v[110:113], v130 offset:59712
	s_waitcnt lgkmcnt(4)
	v_mfma_f32_16x16x32_f16 a[12:15], v[66:69], v[118:121], a[12:15]
	s_waitcnt lgkmcnt(1)
	v_mfma_f32_16x16x32_f16 a[8:11], v[74:77], v[106:109], 0
	ds_read_b128 v[74:77], v130 offset:59776
	v_mfma_f32_16x16x32_f16 a[0:3], v[22:25], v[118:121], a[0:3]
	v_mfma_f32_16x16x32_f16 a[12:15], v[62:65], v[122:125], a[12:15]
	v_mfma_f32_16x16x32_f16 a[4:7], v[2:5], v[118:121], a[4:7]
	s_waitcnt lgkmcnt(1)
	v_mfma_f32_16x16x32_f16 a[8:11], v[70:73], v[110:113], a[8:11]
	ds_read_b128 v[70:73], v130 offset:59840
	s_nop 3
	v_accvgpr_read_b32 v1, a12
	v_mfma_f32_16x16x32_f16 a[0:3], v[18:21], v[122:125], a[0:3]
	v_mfma_f32_16x16x32_f16 a[16:19], v[82:85], v[118:121], a[16:19]
	v_accvgpr_read_b32 v118, a13
	v_accvgpr_read_b32 v119, a14
	v_accvgpr_read_b32 v120, a15
	v_mfma_f32_16x16x32_f16 a[4:7], v[6:9], v[122:125], a[4:7]
	v_cvt_pk_f16_f32 v119, v119, v120
	v_cvt_pk_f16_f32 v118, v1, v118
	s_waitcnt lgkmcnt(1)
	v_mfma_f32_16x16x32_f16 a[8:11], v[66:69], v[74:77], a[8:11]
	v_mfma_f32_16x16x32_f16 a[12:15], v[50:53], v[106:109], 0
	v_accvgpr_read_b32 v50, a0
	v_accvgpr_read_b32 v52, a1
	v_accvgpr_read_b32 v51, a2
	v_accvgpr_read_b32 v53, a3
	s_waitcnt lgkmcnt(0)
	v_mfma_f32_16x16x32_f16 a[8:11], v[62:65], v[70:73], a[8:11]
	v_cvt_pk_f16_f32 v51, v51, v53
	v_cvt_pk_f16_f32 v50, v50, v52
	v_accvgpr_read_b32 v52, a4
	v_mfma_f32_16x16x32_f16 a[12:15], v[78:81], v[110:113], a[12:15]
	v_accvgpr_read_b32 v62, a5
	v_accvgpr_read_b32 v53, a6
	v_accvgpr_read_b32 v63, a7
	v_mfma_f32_16x16x32_f16 a[4:7], v[58:61], v[106:109], 0
	v_cvt_pk_f16_f32 v53, v53, v63
	v_cvt_pk_f16_f32 v52, v52, v62
	v_mfma_f32_16x16x32_f16 a[0:3], v[82:85], v[74:77], a[12:15]
	v_mfma_f32_16x16x32_f16 a[4:7], v[54:57], v[110:113], a[4:7]
	v_mfma_f32_16x16x32_f16 a[16:19], v[86:89], v[122:125], a[16:19]
	v_mfma_f32_16x16x32_f16 a[0:3], v[86:89], v[70:73], a[0:3]
	v_mfma_f32_16x16x32_f16 a[4:7], v[22:25], v[74:77], a[4:7]
	s_nop 5
	v_accvgpr_read_b32 v1, a16
	v_accvgpr_read_b32 v120, a17
	v_accvgpr_read_b32 v66, a18
	v_accvgpr_read_b32 v67, a19
	v_cvt_pk_f16_f32 v67, v66, v67
	v_cvt_pk_f16_f32 v66, v1, v120
	v_add_u32_e32 v1, 0x6000, v131
	ds_write2_b64 v1, v[118:119], v[66:67] offset0:96 offset1:100
	ds_write2_b64 v1, v[50:51], v[52:53] offset0:104 offset1:108
	v_accvgpr_read_b32 v1, a8
	v_accvgpr_read_b32 v50, a9
	v_cvt_pk_f16_f32 v50, v1, v50
	v_accvgpr_read_b32 v1, a0
	v_accvgpr_read_b32 v22, a1
	v_mfma_f32_16x16x32_f16 a[4:7], v[18:21], v[70:73], a[4:7]
	v_accvgpr_read_b32 v18, a2
	v_accvgpr_read_b32 v19, a3
	v_accvgpr_read_b32 v51, a10
	v_mfma_f32_16x16x32_f16 a[0:3], v[14:17], v[106:109], 0
	v_accvgpr_read_b32 v52, a11
	v_cvt_pk_f16_f32 v51, v51, v52
	v_cvt_pk_f16_f32 v19, v18, v19
	v_mfma_f32_16x16x32_f16 a[0:3], v[10:13], v[110:113], a[0:3]
	v_accvgpr_read_b32 v10, a4
	v_accvgpr_read_b32 v11, a5
	v_accvgpr_read_b32 v12, a6
	v_mfma_f32_16x16x32_f16 a[0:3], v[2:5], v[74:77], a[0:3]
	v_accvgpr_read_b32 v2, a7
	v_cvt_pk_f16_f32 v18, v1, v22
	v_add_u32_e32 v1, 0x8000, v131
	v_mfma_f32_16x16x32_f16 a[0:3], v[6:9], v[70:73], a[0:3]
	v_cvt_pk_f16_f32 v3, v12, v2
	v_cvt_pk_f16_f32 v2, v10, v11
	ds_write2_b64 v1, v[50:51], v[18:19] offset0:128 offset1:132
	s_nop 4
	v_accvgpr_read_b32 v4, a0
	v_accvgpr_read_b32 v6, a1
	v_accvgpr_read_b32 v5, a2
	v_accvgpr_read_b32 v7, a3
	v_cvt_pk_f16_f32 v5, v5, v7
	v_cvt_pk_f16_f32 v4, v4, v6
	ds_write2_b64 v1, v[2:3], v[4:5] offset0:136 offset1:140
	global_load_dwordx4 v[2:5], v132, s[10:11] offset:48
	global_load_dwordx4 v[6:9], v132, s[10:11] offset:32
	global_load_dwordx4 v[10:13], v132, s[10:11] offset:16
	global_load_dwordx4 v[14:17], v132, s[10:11]
	global_load_dwordx4 v[18:21], v133, s[6:7] offset:16
	global_load_dwordx4 v[22:25], v133, s[6:7]
	global_load_dword v1, v90, s[8:9]
	s_waitcnt lgkmcnt(0)
	s_barrier
	v_add_u32_e32 v56, 0x1000, v92
	v_add_u32_e32 v57, 0x2000, v92
	v_add_u32_e32 v58, 0x3000, v92
	v_add_u32_e32 v59, 0x4000, v92
	v_add_u32_e32 v60, 0x5000, v92
	global_load_dwordx4 a[36:39], v92, s[4:5]
	global_load_dwordx4 a[68:71], v57, s[4:5]
	global_load_dwordx4 a[24:27], v59, s[4:5]
	global_load_dwordx4 a[40:43], v92, s[4:5] offset:1024
	global_load_dwordx4 a[72:75], v57, s[4:5] offset:1024
	global_load_dwordx4 a[28:31], v59, s[4:5] offset:1024
	global_load_dwordx4 a[44:47], v92, s[4:5] offset:2048
	global_load_dwordx4 a[76:79], v57, s[4:5] offset:2048
	global_load_dwordx4 a[32:35], v59, s[4:5] offset:2048
	global_load_dwordx4 a[48:51], v92, s[4:5] offset:3072
	global_load_dwordx4 a[80:83], v57, s[4:5] offset:3072
	global_load_dwordx4 v[148:151], v59, s[4:5] offset:3072
	global_load_dwordx4 a[52:55], v56, s[4:5]
	global_load_dwordx4 a[84:87], v58, s[4:5]
	global_load_dwordx4 v[152:155], v60, s[4:5]
	global_load_dwordx4 a[56:59], v56, s[4:5] offset:1024
	global_load_dwordx4 a[12:15], v58, s[4:5] offset:1024
	global_load_dwordx4 v[156:159], v60, s[4:5] offset:1024
	global_load_dwordx4 a[60:63], v56, s[4:5] offset:2048
	global_load_dwordx4 a[16:19], v58, s[4:5] offset:2048
	global_load_dwordx4 v[160:163], v60, s[4:5] offset:2048
	global_load_dwordx4 a[64:67], v56, s[4:5] offset:3072
	global_load_dwordx4 a[20:23], v58, s[4:5] offset:3072
	global_load_dwordx4 v[164:167], v60, s[4:5] offset:3072
	ds_read_b128 v[50:53], v93 offset:6864
	ds_read_b128 v[82:85], v93 offset:7392
	ds_read_b128 v[106:109], v93 offset:7920
	ds_read_b128 v[118:121], v93 offset:8448
	ds_read_b128 v[62:65], v93 offset:8976
	ds_read_b128 v[70:73], v93 offset:9504
	ds_read_b128 v[78:81], v93 offset:10032
	ds_read_b128 v[74:77], v93 offset:10560
	s_waitcnt lgkmcnt(7)
	v_cvt_f32_f16_e32 v54, v50
	v_cvt_f32_f16_sdwa v55, v50 dst_sel:DWORD dst_unused:UNUSED_PAD src0_sel:WORD_1
	s_waitcnt lgkmcnt(6)
	v_cvt_f32_f16_e32 v122, v82
	v_cvt_f32_f16_sdwa v123, v82 dst_sel:DWORD dst_unused:UNUSED_PAD src0_sel:WORD_1
	s_waitcnt lgkmcnt(5)
	v_cvt_f32_f16_e32 v110, v106
	v_cvt_f32_f16_sdwa v111, v106 dst_sel:DWORD dst_unused:UNUSED_PAD src0_sel:WORD_1
	s_waitcnt lgkmcnt(4)
	v_cvt_f32_f16_e32 v86, v118
	v_cvt_f32_f16_sdwa v87, v118 dst_sel:DWORD dst_unused:UNUSED_PAD src0_sel:WORD_1
	s_waitcnt vmcnt(31)
	v_pk_fma_f32 v[54:55], v[102:103], v[54:55], v[46:47]
	v_cvt_f32_f16_e32 v126, v83
	v_pk_fma_f32 v[54:55], v[42:43], v[122:123], v[54:55]
	v_cvt_f32_f16_sdwa v127, v83 dst_sel:DWORD dst_unused:UNUSED_PAD src0_sel:WORD_1
	v_pk_fma_f32 v[54:55], v[104:105], v[110:111], v[54:55]
	v_cvt_f32_f16_e32 v112, v107
	v_pk_fma_f32 v[124:125], v[44:45], v[86:87], v[54:55]
	v_cvt_f32_f16_sdwa v55, v51 dst_sel:DWORD dst_unused:UNUSED_PAD src0_sel:WORD_1
	v_mul_f32_e32 v54, 0xbfb8aa3b, v125
	v_exp_f32_e32 v54, v54
	v_cvt_f32_f16_sdwa v113, v107 dst_sel:DWORD dst_unused:UNUSED_PAD src0_sel:WORD_1
	v_cvt_f32_f16_e32 v88, v119
	v_cvt_f32_f16_sdwa v89, v119 dst_sel:DWORD dst_unused:UNUSED_PAD src0_sel:WORD_1
	v_add_f32_e32 v56, 1.0, v54
	v_cvt_f32_f16_e32 v54, v51
	v_mul_f32_e32 v50, 0xbfb8aa3b, v124
	v_exp_f32_e32 v50, v50
	v_cvt_f32_f16_e32 v118, v52
	v_pk_fma_f32 v[54:55], v[98:99], v[54:55], v[48:49]
	v_cvt_f32_f16_sdwa v119, v52 dst_sel:DWORD dst_unused:UNUSED_PAD src0_sel:WORD_1
	v_pk_fma_f32 v[54:55], v[38:39], v[126:127], v[54:55]
	v_add_f32_e32 v50, 1.0, v50
	v_pk_fma_f32 v[54:55], v[100:101], v[112:113], v[54:55]
	v_rcp_f32_e32 v50, v50
	v_pk_fma_f32 v[82:83], v[40:41], v[88:89], v[54:55]
	v_cvt_f32_f16_e32 v144, v108
	v_mul_f32_e32 v51, 0xbfb8aa3b, v82
	v_exp_f32_e32 v54, v51
	v_mul_f32_e32 v51, 0xbfb8aa3b, v83
	v_exp_f32_e32 v55, v51
	v_rcp_f32_e32 v51, v56
	v_add_f32_e32 v54, 1.0, v54
	v_rcp_f32_e32 v106, v54
	v_add_f32_e32 v54, 1.0, v55
	v_rcp_f32_e32 v107, v54
	v_pk_mul_f32 v[50:51], v[124:125], v[50:51]
	v_cvt_f32_f16_e32 v124, v84
	v_cvt_f32_f16_sdwa v125, v84 dst_sel:DWORD dst_unused:UNUSED_PAD src0_sel:WORD_1
	v_cvt_f32_f16_sdwa v145, v108 dst_sel:DWORD dst_unused:UNUSED_PAD src0_sel:WORD_1
	v_pk_mul_f32 v[82:83], v[82:83], v[106:107]
	v_cvt_f32_f16_e32 v106, v120
	v_cvt_f32_f16_sdwa v107, v120 dst_sel:DWORD dst_unused:UNUSED_PAD src0_sel:WORD_1
	v_pk_fma_f32 v[118:119], v[94:95], v[118:119], v[34:35]
	v_cvt_pk_f16_f32 v50, v50, v51
	v_pk_fma_f32 v[118:119], v[30:31], v[124:125], v[118:119]
	v_cvt_f32_f16_e32 v146, v85
	v_pk_fma_f32 v[118:119], v[96:97], v[144:145], v[118:119]
	v_cvt_f32_f16_sdwa v147, v85 dst_sel:DWORD dst_unused:UNUSED_PAD src0_sel:WORD_1
	v_pk_fma_f32 v[118:119], v[32:33], v[106:107], v[118:119]
	v_cvt_f32_f16_e32 v108, v121
	v_mul_f32_e32 v51, 0xbfb8aa3b, v118
	v_exp_f32_e32 v52, v51
	v_mul_f32_e32 v51, 0xbfb8aa3b, v119
	v_exp_f32_e32 v84, v51
	v_cvt_pk_f16_f32 v51, v82, v83
	v_add_f32_e32 v52, 1.0, v52
	v_rcp_f32_e32 v128, v52
	v_add_f32_e32 v52, 1.0, v84
	v_rcp_f32_e32 v129, v52
	v_cvt_f32_f16_e32 v52, v53
	v_cvt_f32_f16_sdwa v53, v53 dst_sel:DWORD dst_unused:UNUSED_PAD src0_sel:WORD_1
	v_mov_b32_e32 v82, v114
	v_mov_b32_e32 v83, v26
	v_mov_b32_e32 v26, v115
	v_cvt_f32_f16_e32 v114, v109
	v_cvt_f32_f16_sdwa v115, v109 dst_sel:DWORD dst_unused:UNUSED_PAD src0_sel:WORD_1
	v_cvt_f32_f16_sdwa v109, v121 dst_sel:DWORD dst_unused:UNUSED_PAD src0_sel:WORD_1
	v_pk_fma_f32 v[52:53], v[82:83], v[52:53], v[36:37]
	v_mov_b32_e32 v84, v116
	v_pk_fma_f32 v[52:53], v[26:27], v[146:147], v[52:53]
	v_mov_b32_e32 v85, v28
	v_pk_fma_f32 v[52:53], v[84:85], v[114:115], v[52:53]
	v_mov_b32_e32 v28, v117
	v_pk_fma_f32 v[116:117], v[28:29], v[108:109], v[52:53]
	s_waitcnt lgkmcnt(3)
	v_cvt_f32_f16_e32 v132, v62
	v_mul_f32_e32 v52, 0xbfb8aa3b, v116
	v_exp_f32_e32 v120, v52
	v_mul_f32_e32 v52, 0xbfb8aa3b, v117
	v_exp_f32_e32 v121, v52
	v_cvt_f32_f16_sdwa v133, v62 dst_sel:DWORD dst_unused:UNUSED_PAD src0_sel:WORD_1
	v_pk_mul_f32 v[52:53], v[118:119], v[128:129]
	v_add_f32_e32 v118, 1.0, v120
	v_add_f32_e32 v119, 1.0, v121
	v_pk_fma_f32 v[120:121], v[102:103], v[122:123], v[46:47]
	v_rcp_f32_e32 v118, v118
	v_pk_fma_f32 v[120:121], v[42:43], v[110:111], v[120:121]
	v_rcp_f32_e32 v119, v119
	v_pk_fma_f32 v[120:121], v[104:105], v[86:87], v[120:121]
	v_cvt_f32_f16_e32 v130, v63
	v_pk_fma_f32 v[120:121], v[44:45], v[132:133], v[120:121]
	v_cvt_f32_f16_sdwa v131, v63 dst_sel:DWORD dst_unused:UNUSED_PAD src0_sel:WORD_1
	v_mul_f32_e32 v62, 0xbfb8aa3b, v120
	v_exp_f32_e32 v62, v62
	v_mul_f32_e32 v122, 0xbfb8aa3b, v121
	v_exp_f32_e32 v123, v122
	v_pk_mul_f32 v[116:117], v[116:117], v[118:119]
	v_add_f32_e32 v62, 1.0, v62
	v_rcp_f32_e32 v122, v62
	v_add_f32_e32 v62, 1.0, v123
	v_rcp_f32_e32 v123, v62
	v_pk_fma_f32 v[62:63], v[98:99], v[126:127], v[48:49]
	v_cvt_pk_f16_f32 v52, v52, v53
	v_pk_fma_f32 v[62:63], v[38:39], v[112:113], v[62:63]
	v_cvt_pk_f16_f32 v53, v116, v117
	v_pk_fma_f32 v[62:63], v[100:101], v[88:89], v[62:63]
	v_pk_mul_f32 v[116:117], v[120:121], v[122:123]
	v_pk_fma_f32 v[118:119], v[40:41], v[130:131], v[62:63]
	v_cvt_f32_f16_e32 v128, v64
	v_mul_f32_e32 v62, 0xbfb8aa3b, v118
	v_exp_f32_e32 v63, v62
	v_mul_f32_e32 v62, 0xbfb8aa3b, v119
	v_exp_f32_e32 v120, v62
	v_cvt_f32_f16_sdwa v129, v64 dst_sel:DWORD dst_unused:UNUSED_PAD src0_sel:WORD_1
	v_add_f32_e32 v63, 1.0, v63
	v_cvt_pk_f16_f32 v62, v116, v117
	v_rcp_f32_e32 v116, v63
	v_add_f32_e32 v63, 1.0, v120
	v_pk_fma_f32 v[120:121], v[94:95], v[124:125], v[34:35]
	v_rcp_f32_e32 v117, v63
	v_pk_fma_f32 v[120:121], v[30:31], v[144:145], v[120:121]
	v_cvt_f32_f16_e32 v126, v65
	v_pk_fma_f32 v[120:121], v[96:97], v[106:107], v[120:121]
	v_cvt_f32_f16_sdwa v127, v65 dst_sel:DWORD dst_unused:UNUSED_PAD src0_sel:WORD_1
	v_pk_fma_f32 v[120:121], v[32:33], v[128:129], v[120:121]
	v_pk_mul_f32 v[116:117], v[118:119], v[116:117]
	v_mul_f32_e32 v63, 0xbfb8aa3b, v120
	v_exp_f32_e32 v63, v63
	v_mul_f32_e32 v64, 0xbfb8aa3b, v121
	v_pk_fma_f32 v[118:119], v[82:83], v[146:147], v[36:37]
	v_exp_f32_e32 v122, v64
	v_pk_fma_f32 v[118:119], v[26:27], v[114:115], v[118:119]
	v_add_f32_e32 v63, 1.0, v63
	v_pk_fma_f32 v[118:119], v[84:85], v[108:109], v[118:119]
	v_rcp_f32_e32 v64, v63
	v_pk_fma_f32 v[118:119], v[28:29], v[126:127], v[118:119]
	v_add_f32_e32 v63, 1.0, v122
	v_mul_f32_e32 v65, 0xbfb8aa3b, v118
	v_exp_f32_e32 v122, v65
	v_mul_f32_e32 v65, 0xbfb8aa3b, v119
	v_exp_f32_e32 v123, v65
	v_rcp_f32_e32 v65, v63
	s_waitcnt lgkmcnt(2)
	v_cvt_f32_f16_e32 v124, v70
	v_cvt_f32_f16_sdwa v125, v70 dst_sel:DWORD dst_unused:UNUSED_PAD src0_sel:WORD_1
	v_add_f32_e32 v63, 1.0, v122
	v_pk_fma_f32 v[110:111], v[102:103], v[110:111], v[46:47]
	v_rcp_f32_e32 v122, v63
	v_add_f32_e32 v63, 1.0, v123
	v_pk_fma_f32 v[110:111], v[42:43], v[86:87], v[110:111]
	v_rcp_f32_e32 v123, v63
	v_pk_fma_f32 v[110:111], v[104:105], v[132:133], v[110:111]
	v_pk_mul_f32 v[64:65], v[120:121], v[64:65]
	v_pk_fma_f32 v[110:111], v[44:45], v[124:125], v[110:111]
	v_cvt_pk_f16_f32 v64, v64, v65
	v_mul_f32_e32 v65, 0xbfb8aa3b, v110
	v_exp_f32_e32 v70, v65
	v_mul_f32_e32 v65, 0xbfb8aa3b, v111
	v_cvt_pk_f16_f32 v63, v116, v117
	v_pk_mul_f32 v[116:117], v[118:119], v[122:123]
	v_exp_f32_e32 v118, v65
	v_add_f32_e32 v70, 1.0, v70
	v_cvt_pk_f16_f32 v65, v116, v117
	v_rcp_f32_e32 v116, v70
	v_add_f32_e32 v70, 1.0, v118
	v_cvt_f32_f16_e32 v122, v71
	v_cvt_f32_f16_sdwa v123, v71 dst_sel:DWORD dst_unused:UNUSED_PAD src0_sel:WORD_1
	v_rcp_f32_e32 v117, v70
	v_pk_fma_f32 v[70:71], v[98:99], v[112:113], v[48:49]
	v_cvt_f32_f16_e32 v120, v72
	v_pk_fma_f32 v[70:71], v[38:39], v[88:89], v[70:71]
	v_cvt_f32_f16_sdwa v121, v72 dst_sel:DWORD dst_unused:UNUSED_PAD src0_sel:WORD_1
	v_pk_fma_f32 v[70:71], v[100:101], v[130:131], v[70:71]
	v_pk_fma_f32 v[86:87], v[102:103], v[86:87], v[46:47]
	v_pk_fma_f32 v[112:113], v[40:41], v[122:123], v[70:71]
	v_pk_fma_f32 v[86:87], v[42:43], v[132:133], v[86:87]
	v_mul_f32_e32 v70, 0xbfb8aa3b, v112
	v_exp_f32_e32 v118, v70
	v_mul_f32_e32 v70, 0xbfb8aa3b, v113
	v_exp_f32_e32 v119, v70
	v_pk_mul_f32 v[70:71], v[110:111], v[116:117]
	v_pk_fma_f32 v[116:117], v[94:95], v[144:145], v[34:35]
	v_add_f32_e32 v110, 1.0, v118
	v_pk_fma_f32 v[116:117], v[30:31], v[106:107], v[116:117]
	v_add_f32_e32 v111, 1.0, v119
	v_pk_fma_f32 v[116:117], v[96:97], v[128:129], v[116:117]
	v_rcp_f32_e32 v110, v110
	v_pk_fma_f32 v[116:117], v[32:33], v[120:121], v[116:117]
	v_rcp_f32_e32 v111, v111
	v_mul_f32_e32 v72, 0xbfb8aa3b, v116
	v_exp_f32_e32 v72, v72
	v_mul_f32_e32 v118, 0xbfb8aa3b, v117
	v_exp_f32_e32 v119, v118
	v_pk_mul_f32 v[110:111], v[112:113], v[110:111]
	v_add_f32_e32 v72, 1.0, v72
	v_rcp_f32_e32 v118, v72
	v_add_f32_e32 v72, 1.0, v119
	v_rcp_f32_e32 v119, v72
	v_cvt_pk_f16_f32 v70, v70, v71
	v_cvt_pk_f16_f32 v71, v110, v111
	v_pk_fma_f32 v[86:87], v[104:105], v[124:125], v[86:87]
	v_pk_mul_f32 v[110:111], v[116:117], v[118:119]
	v_cvt_f32_f16_e32 v118, v73
	v_cvt_f32_f16_sdwa v119, v73 dst_sel:DWORD dst_unused:UNUSED_PAD src0_sel:WORD_1
	v_pk_fma_f32 v[72:73], v[82:83], v[114:115], v[36:37]
	s_waitcnt lgkmcnt(1)
	v_cvt_f32_f16_e32 v116, v78
	v_pk_fma_f32 v[72:73], v[26:27], v[108:109], v[72:73]
	v_cvt_f32_f16_sdwa v117, v78 dst_sel:DWORD dst_unused:UNUSED_PAD src0_sel:WORD_1
	v_pk_fma_f32 v[72:73], v[84:85], v[126:127], v[72:73]
	v_cvt_f32_f16_sdwa v115, v79 dst_sel:DWORD dst_unused:UNUSED_PAD src0_sel:WORD_1
	v_pk_fma_f32 v[112:113], v[28:29], v[118:119], v[72:73]
	v_pk_fma_f32 v[86:87], v[44:45], v[116:117], v[86:87]
	v_mul_f32_e32 v72, 0xbfb8aa3b, v112
	v_exp_f32_e32 v73, v72
	v_mul_f32_e32 v72, 0xbfb8aa3b, v113
	v_exp_f32_e32 v114, v72
	v_cvt_pk_f16_f32 v72, v110, v111
	v_add_f32_e32 v73, 1.0, v73
	v_rcp_f32_e32 v110, v73
	v_add_f32_e32 v73, 1.0, v114
	v_rcp_f32_e32 v111, v73
	v_mul_f32_e32 v73, 0xbfb8aa3b, v86
	v_exp_f32_e32 v73, v73
	v_mul_f32_e32 v78, 0xbfb8aa3b, v87
	v_exp_f32_e32 v114, v78
	v_pk_fma_f32 v[88:89], v[98:99], v[88:89], v[48:49]
	v_add_f32_e32 v73, 1.0, v73
	v_rcp_f32_e32 v78, v73
	v_add_f32_e32 v73, 1.0, v114
	v_cvt_f32_f16_e32 v114, v79
	v_pk_fma_f32 v[88:89], v[38:39], v[130:131], v[88:89]
	v_pk_mul_f32 v[110:111], v[112:113], v[110:111]
	v_pk_fma_f32 v[88:89], v[100:101], v[122:123], v[88:89]
	ds_read_b128 v[66:69], v93 offset:11088
	ds_read_b128 v[58:61], v93 offset:11616
	v_pk_fma_f32 v[88:89], v[40:41], v[114:115], v[88:89]
	ds_read_b128 v[54:57], v93 offset:12144
	v_mul_f32_e32 v79, 0xbfb8aa3b, v88
	v_exp_f32_e32 v112, v79
	v_mul_f32_e32 v79, 0xbfb8aa3b, v89
	v_exp_f32_e32 v113, v79
	v_rcp_f32_e32 v79, v73
	v_add_f32_e32 v73, 1.0, v112
	v_rcp_f32_e32 v112, v73
	v_add_f32_e32 v73, 1.0, v113
	v_rcp_f32_e32 v113, v73
	v_pk_mul_f32 v[78:79], v[86:87], v[78:79]
	v_cvt_pk_f16_f32 v73, v110, v111
	v_cvt_pk_f16_f32 v78, v78, v79
	v_pk_mul_f32 v[86:87], v[88:89], v[112:113]
	v_cvt_f32_f16_e32 v112, v80
	v_cvt_f32_f16_sdwa v113, v80 dst_sel:DWORD dst_unused:UNUSED_PAD src0_sel:WORD_1
	v_pk_fma_f32 v[88:89], v[94:95], v[106:107], v[34:35]
	v_cvt_f32_f16_e32 v110, v81
	v_pk_fma_f32 v[88:89], v[30:31], v[128:129], v[88:89]
	v_cvt_f32_f16_sdwa v111, v81 dst_sel:DWORD dst_unused:UNUSED_PAD src0_sel:WORD_1
	v_pk_fma_f32 v[88:89], v[96:97], v[120:121], v[88:89]
	v_pk_fma_f32 v[128:129], v[94:95], v[128:129], v[34:35]
	v_pk_fma_f32 v[88:89], v[32:33], v[112:113], v[88:89]
	v_pk_fma_f32 v[128:129], v[30:31], v[120:121], v[128:129]
	v_mul_f32_e32 v79, 0xbfb8aa3b, v88
	v_exp_f32_e32 v80, v79
	v_mul_f32_e32 v79, 0xbfb8aa3b, v89
	v_exp_f32_e32 v106, v79
	v_cvt_pk_f16_f32 v79, v86, v87
	v_add_f32_e32 v80, 1.0, v80
	v_rcp_f32_e32 v86, v80
	v_add_f32_e32 v80, 1.0, v106
	v_rcp_f32_e32 v87, v80
	v_pk_fma_f32 v[80:81], v[82:83], v[108:109], v[36:37]
	v_pk_fma_f32 v[128:129], v[96:97], v[112:113], v[128:129]
	v_pk_fma_f32 v[80:81], v[26:27], v[126:127], v[80:81]
	v_pk_fma_f32 v[126:127], v[82:83], v[126:127], v[36:37]
	v_pk_fma_f32 v[80:81], v[84:85], v[118:119], v[80:81]
	v_pk_fma_f32 v[126:127], v[26:27], v[118:119], v[126:127]
	v_pk_fma_f32 v[106:107], v[28:29], v[110:111], v[80:81]
	v_pk_fma_f32 v[126:127], v[84:85], v[110:111], v[126:127]
	v_mul_f32_e32 v80, 0xbfb8aa3b, v106
	v_exp_f32_e32 v108, v80
	v_mul_f32_e32 v80, 0xbfb8aa3b, v107
	v_exp_f32_e32 v109, v80
	v_pk_mul_f32 v[80:81], v[88:89], v[86:87]
	v_add_f32_e32 v86, 1.0, v108
	s_waitcnt lgkmcnt(3)
	v_cvt_f32_f16_e32 v108, v74
	v_add_f32_e32 v87, 1.0, v109
	v_cvt_f32_f16_sdwa v109, v74 dst_sel:DWORD dst_unused:UNUSED_PAD src0_sel:WORD_1
	v_pk_fma_f32 v[88:89], v[102:103], v[132:133], v[46:47]
	v_rcp_f32_e32 v86, v86
	v_pk_fma_f32 v[88:89], v[42:43], v[124:125], v[88:89]
	v_rcp_f32_e32 v87, v87
	v_pk_fma_f32 v[88:89], v[104:105], v[116:117], v[88:89]
	v_cvt_pk_f16_f32 v80, v80, v81
	v_pk_fma_f32 v[88:89], v[44:45], v[108:109], v[88:89]
	v_pk_mul_f32 v[86:87], v[106:107], v[86:87]
	v_mul_f32_e32 v74, 0xbfb8aa3b, v88
	v_exp_f32_e32 v74, v74
	v_mul_f32_e32 v132, 0xbfb8aa3b, v89
	v_exp_f32_e32 v133, v132
	v_cvt_f32_f16_e32 v106, v75
	v_add_f32_e32 v74, 1.0, v74
	v_rcp_f32_e32 v132, v74
	v_add_f32_e32 v74, 1.0, v133
	v_cvt_f32_f16_sdwa v107, v75 dst_sel:DWORD dst_unused:UNUSED_PAD src0_sel:WORD_1
	v_rcp_f32_e32 v133, v74
	v_pk_fma_f32 v[74:75], v[98:99], v[130:131], v[48:49]
	v_cvt_pk_f16_f32 v81, v86, v87
	v_pk_fma_f32 v[74:75], v[38:39], v[122:123], v[74:75]
	v_pk_mul_f32 v[86:87], v[88:89], v[132:133]
	v_pk_fma_f32 v[74:75], v[100:101], v[114:115], v[74:75]
	v_cvt_f32_f16_sdwa v89, v76 dst_sel:DWORD dst_unused:UNUSED_PAD src0_sel:WORD_1
	v_pk_fma_f32 v[130:131], v[40:41], v[106:107], v[74:75]
	v_pk_fma_f32 v[124:125], v[102:103], v[124:125], v[46:47]
	v_mul_f32_e32 v74, 0xbfb8aa3b, v130
	v_exp_f32_e32 v75, v74
	v_mul_f32_e32 v74, 0xbfb8aa3b, v131
	v_exp_f32_e32 v88, v74
	v_cvt_pk_f16_f32 v74, v86, v87
	v_add_f32_e32 v75, 1.0, v75
	v_rcp_f32_e32 v86, v75
	v_add_f32_e32 v75, 1.0, v88
	v_cvt_f32_f16_e32 v88, v76
	v_rcp_f32_e32 v87, v75
	v_pk_fma_f32 v[124:125], v[42:43], v[116:117], v[124:125]
	v_pk_fma_f32 v[120:121], v[94:95], v[120:121], v[34:35]
	v_pk_fma_f32 v[128:129], v[32:33], v[88:89], v[128:129]
	v_pk_mul_f32 v[130:131], v[130:131], v[86:87]
	v_mul_f32_e32 v75, 0xbfb8aa3b, v128
	v_cvt_f32_f16_e32 v86, v77
	v_cvt_f32_f16_sdwa v87, v77 dst_sel:DWORD dst_unused:UNUSED_PAD src0_sel:WORD_1
	v_exp_f32_e32 v75, v75
	v_mul_f32_e32 v76, 0xbfb8aa3b, v129
	v_exp_f32_e32 v132, v76
	v_pk_fma_f32 v[126:127], v[28:29], v[86:87], v[126:127]
	v_add_f32_e32 v75, 1.0, v75
	v_mul_f32_e32 v77, 0xbfb8aa3b, v126
	v_rcp_f32_e32 v76, v75
	v_add_f32_e32 v75, 1.0, v132
	v_exp_f32_e32 v132, v77
	v_mul_f32_e32 v77, 0xbfb8aa3b, v127
	v_exp_f32_e32 v133, v77
	v_rcp_f32_e32 v77, v75
	v_pk_fma_f32 v[124:125], v[104:105], v[108:109], v[124:125]
	v_add_f32_e32 v75, 1.0, v132
	v_rcp_f32_e32 v132, v75
	v_pk_mul_f32 v[76:77], v[128:129], v[76:77]
	s_waitcnt lgkmcnt(2)
	v_cvt_f32_f16_e32 v128, v66
	v_cvt_f32_f16_sdwa v129, v66 dst_sel:DWORD dst_unused:UNUSED_PAD src0_sel:WORD_1
	v_add_f32_e32 v75, 1.0, v133
	v_rcp_f32_e32 v133, v75
	v_cvt_pk_f16_f32 v76, v76, v77
	v_pk_fma_f32 v[124:125], v[44:45], v[128:129], v[124:125]
	v_cvt_pk_f16_f32 v75, v130, v131
	v_mul_f32_e32 v66, 0xbfb8aa3b, v124
	v_exp_f32_e32 v66, v66
	v_mul_f32_e32 v77, 0xbfb8aa3b, v125
	v_exp_f32_e32 v130, v77
	v_pk_mul_f32 v[126:127], v[126:127], v[132:133]
	v_add_f32_e32 v66, 1.0, v66
	v_cvt_pk_f16_f32 v77, v126, v127
	v_rcp_f32_e32 v126, v66
	v_add_f32_e32 v66, 1.0, v130
	v_cvt_f32_f16_e32 v130, v67
	v_cvt_f32_f16_sdwa v131, v67 dst_sel:DWORD dst_unused:UNUSED_PAD src0_sel:WORD_1
	v_rcp_f32_e32 v127, v66
	v_pk_fma_f32 v[66:67], v[98:99], v[122:123], v[48:49]
	v_pk_fma_f32 v[120:121], v[30:31], v[112:113], v[120:121]
	v_pk_fma_f32 v[66:67], v[38:39], v[114:115], v[66:67]
	v_pk_fma_f32 v[120:121], v[96:97], v[88:89], v[120:121]
	v_pk_fma_f32 v[66:67], v[100:101], v[106:107], v[66:67]
	v_pk_fma_f32 v[116:117], v[102:103], v[116:117], v[46:47]
	v_pk_fma_f32 v[122:123], v[40:41], v[130:131], v[66:67]
	v_pk_fma_f32 v[116:117], v[42:43], v[108:109], v[116:117]
	v_mul_f32_e32 v66, 0xbfb8aa3b, v122
	v_exp_f32_e32 v132, v66
	v_mul_f32_e32 v66, 0xbfb8aa3b, v123
	v_exp_f32_e32 v133, v66
	v_pk_mul_f32 v[66:67], v[124:125], v[126:127]
	v_cvt_f32_f16_e32 v126, v68
	v_cvt_f32_f16_sdwa v127, v68 dst_sel:DWORD dst_unused:UNUSED_PAD src0_sel:WORD_1
	v_add_f32_e32 v124, 1.0, v132
	v_add_f32_e32 v125, 1.0, v133
	v_rcp_f32_e32 v124, v124
	v_pk_fma_f32 v[120:121], v[32:33], v[126:127], v[120:121]
	v_rcp_f32_e32 v125, v125
	v_mul_f32_e32 v68, 0xbfb8aa3b, v120
	v_exp_f32_e32 v68, v68
	v_mul_f32_e32 v132, 0xbfb8aa3b, v121
	v_exp_f32_e32 v133, v132
	v_pk_mul_f32 v[122:123], v[122:123], v[124:125]
	v_add_f32_e32 v68, 1.0, v68
	v_rcp_f32_e32 v132, v68
	v_add_f32_e32 v68, 1.0, v133
	v_cvt_pk_f16_f32 v66, v66, v67
	v_cvt_pk_f16_f32 v67, v122, v123
	v_cvt_f32_f16_e32 v122, v69
	v_cvt_f32_f16_sdwa v123, v69 dst_sel:DWORD dst_unused:UNUSED_PAD src0_sel:WORD_1
	v_rcp_f32_e32 v133, v68
	v_pk_fma_f32 v[68:69], v[82:83], v[118:119], v[36:37]
	s_waitcnt lgkmcnt(1)
	v_cvt_f32_f16_sdwa v125, v58 dst_sel:DWORD dst_unused:UNUSED_PAD src0_sel:WORD_1
	v_pk_fma_f32 v[68:69], v[26:27], v[110:111], v[68:69]
	v_pk_mul_f32 v[120:121], v[120:121], v[132:133]
	v_pk_fma_f32 v[68:69], v[84:85], v[86:87], v[68:69]
	v_pk_fma_f32 v[116:117], v[104:105], v[128:129], v[116:117]
	v_pk_fma_f32 v[118:119], v[28:29], v[122:123], v[68:69]
	v_pk_fma_f32 v[114:115], v[98:99], v[114:115], v[48:49]
	v_mul_f32_e32 v68, 0xbfb8aa3b, v118
	v_exp_f32_e32 v69, v68
	v_mul_f32_e32 v68, 0xbfb8aa3b, v119
	v_exp_f32_e32 v124, v68
	v_cvt_pk_f16_f32 v68, v120, v121
	v_add_f32_e32 v69, 1.0, v69
	v_rcp_f32_e32 v120, v69
	v_add_f32_e32 v69, 1.0, v124
	v_rcp_f32_e32 v121, v69
	v_cvt_f32_f16_e32 v124, v58
	v_pk_fma_f32 v[114:115], v[38:39], v[106:107], v[114:115]
	v_pk_fma_f32 v[112:113], v[94:95], v[112:113], v[34:35]
	v_pk_mul_f32 v[118:119], v[118:119], v[120:121]
	v_pk_fma_f32 v[116:117], v[44:45], v[124:125], v[116:117]
	v_cvt_f32_f16_e32 v120, v59
	v_cvt_f32_f16_sdwa v121, v59 dst_sel:DWORD dst_unused:UNUSED_PAD src0_sel:WORD_1
	v_mul_f32_e32 v58, 0xbfb8aa3b, v116
	v_mul_f32_e32 v69, 0xbfb8aa3b, v117
	v_exp_f32_e32 v58, v58
	v_exp_f32_e32 v69, v69
	v_pk_fma_f32 v[114:115], v[100:101], v[130:131], v[114:115]
	v_pk_fma_f32 v[112:113], v[30:31], v[88:89], v[112:113]
	v_pk_fma_f32 v[114:115], v[40:41], v[120:121], v[114:115]
	v_add_f32_e32 v58, 1.0, v58
	v_mul_f32_e32 v59, 0xbfb8aa3b, v114
	v_add_f32_e32 v69, 1.0, v69
	v_exp_f32_e32 v132, v59
	v_mul_f32_e32 v59, 0xbfb8aa3b, v115
	v_rcp_f32_e32 v58, v58
	v_exp_f32_e32 v133, v59
	v_rcp_f32_e32 v59, v69
	v_pk_fma_f32 v[112:113], v[96:97], v[126:127], v[112:113]
	v_add_f32_e32 v69, 1.0, v132
	v_rcp_f32_e32 v132, v69
	v_pk_mul_f32 v[58:59], v[116:117], v[58:59]
	v_cvt_f32_f16_e32 v116, v60
	v_cvt_f32_f16_sdwa v117, v60 dst_sel:DWORD dst_unused:UNUSED_PAD src0_sel:WORD_1
	v_add_f32_e32 v69, 1.0, v133
	v_cvt_pk_f16_f32 v58, v58, v59
	v_rcp_f32_e32 v133, v69
	v_pk_fma_f32 v[112:113], v[32:33], v[116:117], v[112:113]
	v_cvt_pk_f16_f32 v69, v118, v119
	v_mul_f32_e32 v59, 0xbfb8aa3b, v112
	v_exp_f32_e32 v60, v59
	v_mul_f32_e32 v59, 0xbfb8aa3b, v113
	v_exp_f32_e32 v118, v59
	v_pk_mul_f32 v[114:115], v[114:115], v[132:133]
	v_add_f32_e32 v60, 1.0, v60
	v_cvt_pk_f16_f32 v59, v114, v115
	v_rcp_f32_e32 v114, v60
	v_add_f32_e32 v60, 1.0, v118
	v_cvt_f32_f16_e32 v118, v61
	v_cvt_f32_f16_sdwa v119, v61 dst_sel:DWORD dst_unused:UNUSED_PAD src0_sel:WORD_1
	v_rcp_f32_e32 v115, v60
	v_pk_fma_f32 v[60:61], v[82:83], v[110:111], v[36:37]
	v_pk_fma_f32 v[46:47], v[102:103], v[108:109], v[46:47]
	v_pk_fma_f32 v[60:61], v[26:27], v[86:87], v[60:61]
	v_pk_fma_f32 v[42:43], v[42:43], v[128:129], v[46:47]
	v_pk_fma_f32 v[60:61], v[84:85], v[122:123], v[60:61]
	v_pk_fma_f32 v[42:43], v[104:105], v[124:125], v[42:43]
	v_pk_fma_f32 v[110:111], v[28:29], v[118:119], v[60:61]
	v_pk_fma_f32 v[34:35], v[94:95], v[88:89], v[34:35]
	v_mul_f32_e32 v60, 0xbfb8aa3b, v110
	v_exp_f32_e32 v132, v60
	v_mul_f32_e32 v60, 0xbfb8aa3b, v111
	v_exp_f32_e32 v133, v60
	v_pk_mul_f32 v[60:61], v[112:113], v[114:115]
	s_waitcnt lgkmcnt(0)
	v_cvt_f32_f16_e32 v114, v54
	v_cvt_f32_f16_sdwa v115, v54 dst_sel:DWORD dst_unused:UNUSED_PAD src0_sel:WORD_1
	v_add_f32_e32 v112, 1.0, v132
	v_add_f32_e32 v113, 1.0, v133
	v_rcp_f32_e32 v112, v112
	v_pk_fma_f32 v[42:43], v[44:45], v[114:115], v[42:43]
	v_rcp_f32_e32 v113, v113
	v_mul_f32_e32 v44, 0xbfb8aa3b, v42
	v_mul_f32_e32 v45, 0xbfb8aa3b, v43
	v_exp_f32_e32 v44, v44
	v_exp_f32_e32 v45, v45
	v_pk_mul_f32 v[46:47], v[110:111], v[112:113]
	v_cvt_pk_f16_f32 v60, v60, v61
	v_add_f32_e32 v44, 1.0, v44
	v_add_f32_e32 v45, 1.0, v45
	v_rcp_f32_e32 v44, v44
	v_rcp_f32_e32 v45, v45
	v_cvt_pk_f16_f32 v61, v46, v47
	v_pk_fma_f32 v[46:47], v[98:99], v[106:107], v[48:49]
	v_pk_fma_f32 v[30:31], v[30:31], v[126:127], v[34:35]
	v_pk_mul_f32 v[42:43], v[42:43], v[44:45]
	v_cvt_f32_f16_e32 v44, v55
	v_cvt_f32_f16_sdwa v45, v55 dst_sel:DWORD dst_unused:UNUSED_PAD src0_sel:WORD_1
	v_pk_fma_f32 v[38:39], v[38:39], v[130:131], v[46:47]
	v_pk_fma_f32 v[30:31], v[96:97], v[116:117], v[30:31]
	v_pk_fma_f32 v[38:39], v[100:101], v[120:121], v[38:39]
	v_pk_fma_f32 v[36:37], v[82:83], v[86:87], v[36:37]
	v_pk_fma_f32 v[40:41], v[40:41], v[44:45], v[38:39]
	v_cvt_f32_f16_sdwa v45, v56 dst_sel:DWORD dst_unused:UNUSED_PAD src0_sel:WORD_1
	v_mul_f32_e32 v38, 0xbfb8aa3b, v40
	v_exp_f32_e32 v39, v38
	v_mul_f32_e32 v38, 0xbfb8aa3b, v41
	v_exp_f32_e32 v44, v38
	v_cvt_pk_f16_f32 v38, v42, v43
	v_add_f32_e32 v39, 1.0, v39
	v_rcp_f32_e32 v42, v39
	v_add_f32_e32 v39, 1.0, v44
	v_cvt_f32_f16_e32 v44, v56
	v_rcp_f32_e32 v43, v39
	v_pk_fma_f32 v[26:27], v[26:27], v[122:123], v[36:37]
	v_pk_fma_f32 v[30:31], v[32:33], v[44:45], v[30:31]
	v_pk_fma_f32 v[26:27], v[84:85], v[118:119], v[26:27]
	v_mul_f32_e32 v32, 0xbfb8aa3b, v30
	v_exp_f32_e32 v34, v32
	v_mul_f32_e32 v32, 0xbfb8aa3b, v31
	v_exp_f32_e32 v35, v32
	v_pk_mul_f32 v[32:33], v[40:41], v[42:43]
	v_cvt_f32_f16_e32 v40, v57
	v_cvt_f32_f16_sdwa v41, v57 dst_sel:DWORD dst_unused:UNUSED_PAD src0_sel:WORD_1
	v_add_f32_e32 v34, 1.0, v34
	v_add_f32_e32 v35, 1.0, v35
	v_rcp_f32_e32 v34, v34
	v_pk_fma_f32 v[26:27], v[28:29], v[40:41], v[26:27]
	v_rcp_f32_e32 v35, v35
	v_mul_f32_e32 v28, 0xbfb8aa3b, v26
	v_mul_f32_e32 v29, 0xbfb8aa3b, v27
	v_exp_f32_e32 v28, v28
	v_exp_f32_e32 v29, v29
	v_pk_mul_f32 v[30:31], v[30:31], v[34:35]
	v_cvt_pk_f16_f32 v39, v32, v33
	v_add_f32_e32 v28, 1.0, v28
	v_add_f32_e32 v29, 1.0, v29
	v_rcp_f32_e32 v28, v28
	v_rcp_f32_e32 v29, v29
	v_cvt_pk_f16_f32 v40, v30, v31
	s_barrier
	v_pk_mul_f32 v[26:27], v[26:27], v[28:29]
	v_or_b32_e32 v34, v141, v140
	v_cvt_pk_f16_f32 v41, v26, v27
	ds_write_b128 v93, v[50:53] offset:8448
	ds_write_b128 v93, v[62:65] offset:8976
	ds_write_b128 v93, v[70:73] offset:9504
	ds_write_b128 v93, v[78:81] offset:10032
	ds_write_b128 v93, v[74:77] offset:10560
	ds_write_b128 v93, v[66:69] offset:11088
	ds_write_b128 v93, v[58:61] offset:11616
	ds_write_b128 v93, v[38:41] offset:12144
	v_mov_b32_e32 v93, v91
	v_lshl_add_u64 v[58:59], s[4:5], 0, v[92:93]
	v_add_co_u32_e32 v60, vcc, s17, v58
	s_waitcnt lgkmcnt(0)
	s_nop 0
	v_addc_co_u32_e32 v61, vcc, 0, v59, vcc
	s_barrier
	s_movk_i32 s6, 0x210
	v_add_u32_e32 v34, 16, v34
	v_mad_u32_u24 v66, v34, s6, v142
	ds_read_b128 v[44:47], v66
	ds_read_b128 v[48:51], v66 offset:64
	ds_read_b128 v[52:55], v66 offset:128
	ds_read_b128 v[68:71], v66 offset:192
	ds_read_b128 v[72:75], v66 offset:256
	ds_read_b128 v[76:79], v66 offset:320
	ds_read_b128 v[80:83], v66 offset:384
	ds_read_b128 v[84:87], v66 offset:448
	s_mov_b32 s3, 4
	s_waitcnt vmcnt(0)
	s_waitcnt lgkmcnt(7)
	v_mfma_f32_16x16x32_f16 a[0:3], v[44:47], a[36:39], 0
	v_mfma_f32_16x16x32_f16 a[4:7], v[44:47], a[68:71], 0
	v_mfma_f32_16x16x32_f16 a[8:11], v[44:47], a[24:27], 0
	s_waitcnt lgkmcnt(6)
	v_mfma_f32_16x16x32_f16 a[0:3], v[48:51], a[40:43], a[0:3]
	v_mfma_f32_16x16x32_f16 a[4:7], v[48:51], a[72:75], a[4:7]
	v_mfma_f32_16x16x32_f16 a[8:11], v[48:51], a[28:31], a[8:11]
	s_waitcnt lgkmcnt(5)
	v_mfma_f32_16x16x32_f16 a[0:3], v[52:55], a[44:47], a[0:3]
	v_mfma_f32_16x16x32_f16 a[4:7], v[52:55], a[76:79], a[4:7]
	v_mfma_f32_16x16x32_f16 a[8:11], v[52:55], a[32:35], a[8:11]
	s_waitcnt lgkmcnt(4)
	v_mfma_f32_16x16x32_f16 a[0:3], v[68:71], a[48:51], a[0:3]
	v_mfma_f32_16x16x32_f16 a[4:7], v[68:71], a[80:83], a[4:7]
	v_mfma_f32_16x16x32_f16 a[8:11], v[68:71], v[148:151], a[8:11]
	s_waitcnt lgkmcnt(3)
	v_mfma_f32_16x16x32_f16 a[0:3], v[72:75], a[52:55], a[0:3]
	v_mfma_f32_16x16x32_f16 a[4:7], v[72:75], a[84:87], a[4:7]
	v_mfma_f32_16x16x32_f16 a[8:11], v[72:75], v[152:155], a[8:11]
	s_waitcnt lgkmcnt(2)
	v_mfma_f32_16x16x32_f16 a[0:3], v[76:79], a[56:59], a[0:3]
	v_mfma_f32_16x16x32_f16 a[4:7], v[76:79], a[12:15], a[4:7]
	v_mfma_f32_16x16x32_f16 a[8:11], v[76:79], v[156:159], a[8:11]
	s_waitcnt lgkmcnt(1)
	v_mfma_f32_16x16x32_f16 a[0:3], v[80:83], a[60:63], a[0:3]
	v_mfma_f32_16x16x32_f16 a[4:7], v[80:83], a[16:19], a[4:7]
	v_mfma_f32_16x16x32_f16 a[8:11], v[80:83], v[160:163], a[8:11]
	s_load_dwordx2 s[16:17], s[0:1], 0x60
	s_load_dwordx8 s[4:11], s[0:1], 0x40
	s_movk_i32 s0, 0xd0
	v_mov_b32_e32 v40, v91
	v_mov_b32_e32 v41, v91
	v_mov_b32_e32 v38, v91
	v_mov_b32_e32 v42, v91
	v_mov_b32_e32 v43, v91
	v_mov_b32_e32 v39, v91
	v_lshlrev_b32_e32 v34, 2, v140
	v_or_b32_e32 v35, 0xfa00, v34
	s_waitcnt lgkmcnt(0)
	v_mfma_f32_16x16x32_f16 a[0:3], v[84:87], a[64:67], a[0:3]
	v_mfma_f32_16x16x32_f16 a[4:7], v[84:87], a[20:23], a[4:7]
	v_bitop3_b32 v26, v138, 12, 48 bitop3:0xe0
	v_mad_u32_u24 v26, v26, s0, v35
	v_or_b32_e32 v28, s14, v134
	v_mfma_f32_16x16x32_f16 a[8:11], v[84:87], v[164:167], a[8:11]
	s_nop 7
	s_nop 7
	ds_write_b32 v26, a0
	ds_write_b32 v26, a1 offset:208
	ds_write_b32 v26, a2 offset:416
	ds_write_b32 v26, a3 offset:624
	ds_write_b32 v26, a4 offset:64
	ds_write_b32 v26, a5 offset:272
	ds_write_b32 v26, a6 offset:480
	ds_write_b32 v26, a7 offset:688
	ds_write_b32 v26, a8 offset:128
	ds_write_b32 v26, a9 offset:336
	ds_write_b32 v26, a10 offset:544
	ds_write_b32 v26, a11 offset:752
	v_mad_u32_u24 v26, v134, s0, v35
	s_waitcnt lgkmcnt(0)
	s_barrier
	ds_read2_b32 v[26:27], v26 offset0:8 offset1:24
	v_mov_b32_e32 v29, s15
	v_lshlrev_b64 v[30:31], 6, v[28:29]
	v_or_b32_e32 v30, v30, v34
	v_lshl_add_u64 v[32:33], s[6:7], 0, v[30:31]
	s_waitcnt lgkmcnt(0)
	global_store_dword v[32:33], v26, off sc1
	v_lshl_add_u64 v[30:31], s[8:9], 0, v[30:31]
	v_mad_u32_u24 v26, v135, s0, v35
	global_store_dword v[30:31], v27, off sc1
	ds_read2_b32 v[26:27], v26 offset0:8 offset1:24
	v_or_b32_e32 v28, s14, v135
	v_lshlrev_b64 v[30:31], 6, v[28:29]
	v_or_b32_e32 v30, v30, v34
	v_lshl_add_u64 v[32:33], s[6:7], 0, v[30:31]
	s_waitcnt lgkmcnt(0)
	global_store_dword v[32:33], v26, off sc1
	v_lshl_add_u64 v[30:31], s[8:9], 0, v[30:31]
	v_mad_u32_u24 v26, v136, s0, v35
	global_store_dword v[30:31], v27, off sc1
	ds_read2_b32 v[26:27], v26 offset0:8 offset1:24
	v_or_b32_e32 v28, s14, v136
	v_lshlrev_b64 v[30:31], 6, v[28:29]
	v_or_b32_e32 v30, v30, v34
	v_lshl_add_u64 v[32:33], s[6:7], 0, v[30:31]
	s_waitcnt lgkmcnt(0)
	global_store_dword v[32:33], v26, off sc1
	v_lshl_add_u64 v[30:31], s[8:9], 0, v[30:31]
	v_mad_u32_u24 v26, v137, s0, v35
	global_store_dword v[30:31], v27, off sc1
	ds_read2_b32 v[30:31], v26 offset0:8 offset1:24
	v_or_b32_e32 v28, s14, v137
	v_lshlrev_b64 v[32:33], 6, v[28:29]
	ds_read_b128 v[26:29], v91 offset:64000
	v_or_b32_e32 v32, v32, v34
	v_lshl_add_u64 v[34:35], s[6:7], 0, v[32:33]
	v_lshl_add_u64 v[32:33], s[8:9], 0, v[32:33]
	s_waitcnt lgkmcnt(1)
	global_store_dword v[34:35], v30, off sc1
	global_store_dword v[32:33], v31, off sc1
	ds_read_b128 v[30:33], v91 offset:64016
	v_lshlrev_b32_e32 v46, 1, v0
	ds_read_u16 v48, v46 offset:8448
	s_waitcnt lgkmcnt(2)
	v_fma_f32 v26, v22, v26, v1
	v_fmac_f32_e32 v26, v24, v28
	v_mul_f32_e32 v28, v25, v29
	v_fmac_f32_e32 v28, v23, v27
	s_waitcnt lgkmcnt(1)
	v_fmac_f32_e32 v26, v18, v30
	v_fmac_f32_e32 v28, v19, v31
	v_fmac_f32_e32 v26, v20, v32
	v_fmac_f32_e32 v28, v21, v33
	v_add_f32_e32 v28, v26, v28
	v_mul_f32_e64 v26, |v28|, s18
	v_exp_f32_e32 v26, v26
	s_lshl_b64 s[0:1], s[14:15], 10
	s_add_u32 s0, s4, s0
	s_addc_u32 s1, s5, s1
	v_add_f32_e32 v26, 1.0, v26
	v_log_f32_e32 v29, v26
	v_max_f32_e32 v49, 0, v28
	v_lshl_add_u64 v[26:27], s[0:1], 0, v[90:91]
	v_mul_u32_u24_e32 v164, 12, v0
	v_mov_b32_e32 v165, 0
	v_lshl_add_u64 v[26:27], v[26:27], 0, v[164:165]
	s_mov_b32 s4, 0x3f317218
	v_fmac_f32_e32 v49, 0x3f317218, v29
	v_add_u32_e32 v47, 0x2310, v46
	s_mov_b64 s[0:1], 0
	s_mov_b32 s5, 0xfa20
	v_mov_b32_e32 v28, v91
	v_mov_b32_e32 v29, v91
	v_mov_b32_e32 v36, v91
	v_mov_b32_e32 v37, v91
	v_mov_b32_e32 v34, v91
	v_mov_b32_e32 v35, v91
	v_mov_b32_e32 v32, v91
	v_mov_b32_e32 v33, v91
	v_mov_b32_e32 v30, v91
	v_mov_b32_e32 v31, v91

	.amdhsa_kernel _Z7k_frontPKDF16_S0_PKfS2_S0_S2_S2_S2_PjPfS4_S4_S4_
		.amdhsa_group_segment_fixed_size 77312
		.amdhsa_private_segment_fixed_size 0
		.amdhsa_kernarg_size 104
		.amdhsa_user_sgpr_count 2
		.amdhsa_user_sgpr_dispatch_ptr 0
		.amdhsa_user_sgpr_queue_ptr 0
		.amdhsa_user_sgpr_kernarg_segment_ptr 1
		.amdhsa_user_sgpr_dispatch_id 0
		.amdhsa_user_sgpr_kernarg_preload_length 0
		.amdhsa_user_sgpr_kernarg_preload_offset 0
		.amdhsa_user_sgpr_private_segment_size 0
		.amdhsa_uses_dynamic_stack 0
		.amdhsa_enable_private_segment 0
		.amdhsa_system_sgpr_workgroup_id_x 1
		.amdhsa_system_sgpr_workgroup_id_y 1
		.amdhsa_system_sgpr_workgroup_id_z 0
		.amdhsa_system_sgpr_workgroup_info 0
		.amdhsa_system_vgpr_workitem_id 0
		.amdhsa_next_free_vgpr 256
		.amdhsa_next_free_sgpr 96
		.amdhsa_accum_offset 168
		.amdhsa_reserve_vcc 1
		.amdhsa_float_round_mode_32 0
		.amdhsa_float_round_mode_16_64 0
		.amdhsa_float_denorm_mode_32 3
		.amdhsa_float_denorm_mode_16_64 3
		.amdhsa_dx10_clamp 1
		.amdhsa_ieee_mode 1
		.amdhsa_fp16_overflow 0
		.amdhsa_tg_split 0
		.amdhsa_exception_fp_ieee_invalid_op 0
		.amdhsa_exception_fp_denorm_src 0
		.amdhsa_exception_fp_ieee_div_zero 0
		.amdhsa_exception_fp_ieee_overflow 0
		.amdhsa_exception_fp_ieee_underflow 0
		.amdhsa_exception_fp_ieee_inexact 0
		.amdhsa_exception_int_div_zero 0
	.end_amdhsa_kernel

amdhsa.kernels:
  - .agpr_count:     0
    .args:
      - .actual_access:  read_only
        .address_space:  global
        .offset:         0
        .size:           8
        .value_kind:     global_buffer
      - .actual_access:  read_only
        .address_space:  global
        .offset:         8
        .size:           8
        .value_kind:     global_buffer
      - .actual_access:  read_only
        .address_space:  global
        .offset:         16
        .size:           8
        .value_kind:     global_buffer
      - .actual_access:  write_only
        .address_space:  global
        .offset:         24
        .size:           8
        .value_kind:     global_buffer
      - .actual_access:  write_only
        .address_space:  global
        .offset:         32
        .size:           8
        .value_kind:     global_buffer
      - .actual_access:  write_only
        .address_space:  global
        .offset:         40
        .size:           8
        .value_kind:     global_buffer
      - .offset:         48
        .size:           104
        .value_kind:     by_value
    .group_segment_fixed_size: 37248
    .kernarg_segment_align: 8
    .kernarg_segment_size: 152
    .language:       OpenCL C
    .language_version:
      - 2
      - 0
    .max_flat_workgroup_size: 512
    .name:           _Z4k_lnPKfS0_S0_PDF16_PfS2_7CvtArgs
    .private_segment_fixed_size: 0
    .sgpr_count:     40
    .sgpr_spill_count: 0
    .symbol:         _Z4k_lnPKfS0_S0_PDF16_PfS2_7CvtArgs.kd
    .uniform_work_group_size: 1
    .uses_dynamic_stack: false
    .vgpr_count:     118
    .vgpr_spill_count: 0
    .wavefront_size: 64
  - .agpr_count:     88
    .args:
      - .actual_access:  read_only
        .address_space:  global
        .offset:         0
        .size:           8
        .value_kind:     global_buffer
      - .actual_access:  read_only
        .address_space:  global
        .offset:         8
        .size:           8
        .value_kind:     global_buffer
      - .actual_access:  read_only
        .address_space:  global
        .offset:         16
        .size:           8
        .value_kind:     global_buffer
      - .actual_access:  read_only
        .address_space:  global
        .offset:         24
        .size:           8
        .value_kind:     global_buffer
      - .actual_access:  read_only
        .address_space:  global
        .offset:         32
        .size:           8
        .value_kind:     global_buffer
      - .actual_access:  read_only
        .address_space:  global
        .offset:         40
        .size:           8
        .value_kind:     global_buffer
      - .actual_access:  read_only
        .address_space:  global
        .offset:         48
        .size:           8
        .value_kind:     global_buffer
      - .actual_access:  read_only
        .address_space:  global
        .offset:         56
        .size:           8
        .value_kind:     global_buffer
      - .actual_access:  write_only
        .address_space:  global
        .offset:         64
        .size:           8
        .value_kind:     global_buffer
      - .actual_access:  write_only
        .address_space:  global
        .offset:         72
        .size:           8
        .value_kind:     global_buffer
      - .actual_access:  write_only
        .address_space:  global
        .offset:         80
        .size:           8
        .value_kind:     global_buffer
      - .actual_access:  write_only
        .address_space:  global
        .offset:         88
        .size:           8
        .value_kind:     global_buffer
      - .actual_access:  write_only
        .address_space:  global
        .offset:         96
        .size:           8
        .value_kind:     global_buffer
    .group_segment_fixed_size: 77312
    .kernarg_segment_align: 8
    .kernarg_segment_size: 104
    .language:       OpenCL C
    .language_version:
      - 2
      - 0
    .max_flat_workgroup_size: 256
    .name:           _Z7k_frontPKDF16_S0_PKfS2_S0_S2_S2_S2_PjPfS4_S4_S4_
    .private_segment_fixed_size: 0
    .sgpr_count:     25
    .sgpr_spill_count: 0
    .symbol:         _Z7k_frontPKDF16_S0_PKfS2_S0_S2_S2_S2_PjPfS4_S4_S4_.kd
    .uniform_work_group_size: 1
    .uses_dynamic_stack: false
    .vgpr_count:     256
    .vgpr_spill_count: 0
    .wavefront_size: 64
  - .agpr_count:     0
    .args:
      - .actual_access:  read_only
        .address_space:  global
        .offset:         0
        .size:           8
        .value_kind:     global_buffer
      - .address_space:  global
        .offset:         8
        .size:           8
        .value_kind:     global_buffer
      - .actual_access:  read_only
        .address_space:  global
        .offset:         16
        .size:           8
        .value_kind:     global_buffer
    .group_segment_fixed_size: 0
    .kernarg_segment_align: 8
    .kernarg_segment_size: 24
    .language:       OpenCL C
    .language_version:
      - 2
      - 0
    .max_flat_workgroup_size: 64
    .name:           _Z7k_scan2PKfPfS0_
    .private_segment_fixed_size: 0
    .sgpr_count:     48
    .sgpr_spill_count: 0
    .symbol:         _Z7k_scan2PKfPfS0_.kd
    .uniform_work_group_size: 1
    .uses_dynamic_stack: false
    .vgpr_count:     150
    .vgpr_spill_count: 0
    .wavefront_size: 64
  - .agpr_count:     0
    .args:
      - .actual_access:  read_only
        .address_space:  global
        .offset:         0
        .size:           8
        .value_kind:     global_buffer
      - .actual_access:  read_only
        .address_space:  global
        .offset:         8
        .size:           8
        .value_kind:     global_buffer
      - .actual_access:  read_only
        .address_space:  global
        .offset:         16
        .size:           8
        .value_kind:     global_buffer
      - .actual_access:  read_only
        .address_space:  global
        .offset:         24
        .size:           8
        .value_kind:     global_buffer
      - .actual_access:  read_only
        .address_space:  global
        .offset:         32
        .size:           8
        .value_kind:     global_buffer
      - .actual_access:  read_only
        .address_space:  global
        .offset:         40
        .size:           8
        .value_kind:     global_buffer
      - .actual_access:  read_only
        .address_space:  global
        .offset:         48
        .size:           8
        .value_kind:     global_buffer
      - .actual_access:  read_only
        .address_space:  global
        .offset:         56
        .size:           8
        .value_kind:     global_buffer
      - .actual_access:  read_only
        .address_space:  global
        .offset:         64
        .size:           8
        .value_kind:     global_buffer
      - .offset:         72
        .size:           72
        .value_kind:     by_value
    .group_segment_fixed_size: 60416
    .kernarg_segment_align: 8
    .kernarg_segment_size: 144
    .language:       OpenCL C
    .language_version:
      - 2
      - 0
    .max_flat_workgroup_size: 256
    .name:           _Z7k_scan3PKjPKfS2_S2_S2_S2_PKDF16_S4_S4_7EpiArgs
    .private_segment_fixed_size: 0
    .sgpr_count:     34
    .sgpr_spill_count: 0
    .symbol:         _Z7k_scan3PKjPKfS2_S2_S2_S2_PKDF16_S4_S4_7EpiArgs.kd
    .uniform_work_group_size: 1
    .uses_dynamic_stack: false
    .vgpr_count:     236
    .vgpr_spill_count: 0
    .wavefront_size: 64
  - .agpr_count:     0
    .args:
      - .actual_access:  read_only
        .address_space:  global
        .offset:         0
        .size:           8
        .value_kind:     global_buffer
      - .actual_access:  read_only
        .address_space:  global
        .offset:         8
        .size:           8
        .value_kind:     global_buffer
      - .actual_access:  read_only
        .address_space:  global
        .offset:         16
        .size:           8
        .value_kind:     global_buffer
      - .actual_access:  write_only
        .address_space:  global
        .offset:         24
        .size:           8
        .value_kind:     global_buffer
    .group_segment_fixed_size: 20160
    .kernarg_segment_align: 8
    .kernarg_segment_size: 32
    .language:       OpenCL C
    .language_version:
      - 2
      - 0
    .max_flat_workgroup_size: 256
    .name:           _Z8k_dwconvPKDF16_PKfS2_PDF16_
    .private_segment_fixed_size: 0
    .sgpr_count:     86
    .sgpr_spill_count: 0
    .symbol:         _Z8k_dwconvPKDF16_PKfS2_PDF16_.kd
    .uniform_work_group_size: 1
    .uses_dynamic_stack: false
    .vgpr_count:     65
    .vgpr_spill_count: 0
    .wavefront_size: 64
  - .agpr_count:     0
    .args:
      - .actual_access:  read_only
        .address_space:  global
        .offset:         0
        .size:           8
        .value_kind:     global_buffer
      - .offset:         8
        .size:           72
        .value_kind:     by_value
    .group_segment_fixed_size: 38912
    .kernarg_segment_align: 8
    .kernarg_segment_size: 80
    .language:       OpenCL C
    .language_version:
      - 2
      - 0
    .max_flat_workgroup_size: 256
    .name:           _Z9k_gemm_tlILi2ELb1EEvPKDF16_6TlArgs
    .private_segment_fixed_size: 0
    .sgpr_count:     27
    .sgpr_spill_count: 0
    .symbol:         _Z9k_gemm_tlILi2ELb1EEvPKDF16_6TlArgs.kd
    .uniform_work_group_size: 1
    .uses_dynamic_stack: false
    .vgpr_count:     124
    .vgpr_spill_count: 0
    .wavefront_size: 64
  - .agpr_count:     0
    .args:
      - .actual_access:  read_only
        .address_space:  global
        .offset:         0
        .size:           8
        .value_kind:     global_buffer
      - .offset:         8
        .size:           72
        .value_kind:     by_value
    .group_segment_fixed_size: 34816
    .kernarg_segment_align: 8
    .kernarg_segment_size: 80
    .language:       OpenCL C
    .language_version:
      - 2
      - 0
    .max_flat_workgroup_size: 256
    .name:           _Z9k_gemm_tlILi3ELb0EEvPKDF16_6TlArgs
    .private_segment_fixed_size: 0
    .sgpr_count:     18
    .sgpr_spill_count: 0
    .symbol:         _Z9k_gemm_tlILi3ELb0EEvPKDF16_6TlArgs.kd
    .uniform_work_group_size: 1
    .uses_dynamic_stack: false
    .vgpr_count:     110
    .vgpr_spill_count: 0
    .wavefront_size: 64
